# GLA chunk top: next-chunk prefetch offsets derived incrementally from the steps; full row recomputation only at chunk 0 and the context->latent transition
# baseline (speedup 1.0000x reference)
.LBB0_469:
	s_cmpk_eq_i32 s91, 0x8c0
	s_cbranch_scc1 .Lgp_last
	s_cmp_eq_u32 s92, 0
	s_cbranch_scc1 .Lgp_full
	s_cmp_lg_u32 s92, 3
	s_cbranch_scc1 .Lgp_fast
.Lgp_full:
	s_cmp_gt_u32 s92, 2
	s_cselect_b64 s[0:1], -1, 0
	s_mov_b64 s[36:37], -1
	s_and_b64 vcc, exec, s[0:1]
	s_cbranch_vccnz .Lgp_490
	s_andn2_b64 vcc, exec, s[36:37]
	s_cbranch_vccz .Lgp_491

.Lgp_fast:
	s_cmp_lt_u32 s92, 4
	s_cbranch_scc1 .Lgp_lin
	s_bitcmp1_b32 s38, 0
	s_cbranch_scc1 .Lgp_lin
	s_ashr_i32 s0, s98, 5
	s_lshl_b32 s1, s98, 3
	s_sub_i32 s0, s0, s1
	v_add_u32_e32 v210, s0, v210
	s_ashr_i32 s0, s99, 5
	s_lshl_b32 s1, s99, 3
	s_sub_i32 s0, s0, s1
	v_add_u32_e32 v211, s0, v211
	s_ashr_i32 s0, s100, 5
	s_lshl_b32 s1, s100, 4
	s_sub_i32 s0, s0, s1
	v_add_u32_e32 v214, s0, v214
	s_branch .Lgp_skip
.Lgp_lin:
	s_mul_i32 s0, s98, 56
	v_add_u32_e32 v210, s0, v210
	s_mul_i32 s0, s99, 56
	v_add_u32_e32 v211, s0, v211
	s_mul_i32 s0, s100, 48
	v_add_u32_e32 v214, s0, v214
	s_branch .Lgp_skip
